# MoE GEMMs: each XCD walks a contiguous range of expert row panels (weight tiles reused from its L2 across rounds; GU panel consumed by the XCD that produced it) instead of every 8th panel group (on to
# speedup vs baseline: 1.0078x; 1.0078x over previous
.LBB0_1973:
	s_andn2_b64 vcc, exec, s[6:7]
	v_readlane_b32 s8, v253, 15
	v_readlane_b32 s9, v253, 16
	s_cbranch_vccnz .LBB0_1975
	v_readlane_b32 s100, v252, 59
	s_add_i32 s101, s10, 7
	s_lshr_b32 s101, s101, 3
	s_and_b32 vcc_lo, s100, 3
	s_lshr_b32 s100, s100, 2
	s_mul_i32 s100, s100, s101
	s_add_i32 s9, s100, vcc_lo
	s_cmp_lt_i32 vcc_lo, s101
	s_cselect_b32 s101, s10, 0
	s_cmp_lt_i32 s9, s101
	s_cselect_b64 s[4:5], -1, 0
	v_readlane_b32 s8, v252, 60

.LBB0_1991:
	v_readlane_b32 s100, v252, 59
	s_add_i32 s101, s26, 7
	s_lshr_b32 s101, s101, 3
	s_and_b32 vcc_lo, s100, 3
	s_lshl_b32 vcc_hi, s31, 2
	s_add_i32 vcc_lo, vcc_lo, vcc_hi
	s_lshr_b32 s100, s100, 2
	s_mul_i32 s100, s100, s101
	s_add_i32 s40, s100, vcc_lo
	s_cmp_lt_i32 vcc_lo, s101
	s_cselect_b32 s101, s26, 0
	s_cmp_lt_i32 s40, s101
	v_readlane_b32 s26, v252, 60
	s_cselect_b64 s[0:1], -1, 0
	s_mov_b32 s42, s26
	s_andn2_b64 vcc, exec, s[0:1]
	s_mov_b64 s[52:53], 0
	s_cbranch_vccz .LBB0_1994
	s_branch .LBB0_1995

.LBB0_2066:
	s_andn2_b64 vcc, exec, s[6:7]
	v_readlane_b32 s6, v252, 61
	s_mov_b32 s40, s6
	v_readlane_b32 s6, v253, 21
	s_mov_b32 s36, s6
	s_cbranch_vccnz .LBB0_2068
	v_readlane_b32 s100, v252, 62
	s_add_i32 s101, s9, 7
	s_lshr_b32 s101, s101, 3
	s_and_b32 vcc_lo, s100, 7
	s_lshr_b32 s100, s100, 3
	s_mul_i32 s100, s100, s101
	s_add_i32 s40, s100, vcc_lo
	s_cmp_lt_i32 vcc_lo, s101
	s_cselect_b32 s101, s9, 0
	s_cmp_lt_i32 s40, s101
	v_readlane_b32 s6, v252, 63
	s_cselect_b64 s[4:5], -1, 0
	s_mov_b32 s36, s6

.LBB0_2080:
	v_readlane_b32 s100, v252, 62
	s_add_i32 s101, s13, 7
	s_lshr_b32 s101, s101, 3
	s_and_b32 vcc_lo, s100, 7
	s_lshl_b32 vcc_hi, s23, 3
	s_add_i32 vcc_lo, vcc_lo, vcc_hi
	s_lshr_b32 s100, s100, 3
	s_mul_i32 s100, s100, s101
	s_add_i32 s12, s100, vcc_lo
	s_cmp_lt_i32 vcc_lo, s101
	s_cselect_b32 s101, s13, 0
	s_cmp_lt_i32 s12, s101
	v_readlane_b32 s13, v252, 63
	s_cselect_b64 s[0:1], -1, 0
	s_mov_b32 s28, s13
	s_andn2_b64 vcc, exec, s[0:1]
	s_mov_b64 s[48:49], 0
	s_cbranch_vccz .LBB0_2083
	s_branch .LBB0_2084
